# router logits loop fully unrolled with the next trip's w_router loads in flight under the current MFMAs (on top of the m=7 boundary-pipelined version)
# baseline (speedup 1.0000x reference)
; #define LAS __attribute__((address_space(3)))
; __device__ __forceinline__ void phase_router(const Args& a, LAS unsigned char* lds) {
;     ...
;                 const int kk = lane >> 4, fr = lane & 15;
;                 f32x4 acc0 = {0.f, 0.f, 0.f, 0.f}, acc1 = {0.f, 0.f, 0.f, 0.f};
;                 const float* wp = a.w_router + (size_t)(w * 256 + kk) * 32 + fr; const LAS float* hp = h2s + fr * HS + w * 256 + kk;
; #pragma unroll 8
;                 for (int ks = 0; ks < 64; ++ks) { const float b = hp[ks * 4], a0 = wp[(size_t)ks * 128], a1 = wp[(size_t)ks * 128 + 16];
;                     acc0 = __builtin_amdgcn_mfma_f32_16x16x4f32(a0, b, acc0, 0, 0, 0); acc1 = __builtin_amdgcn_mfma_f32_16x16x4f32(a1, b, acc1, 0, 0, 0); }
; #pragma unroll
;                 for (int r = 0; r < 4; ++r) { part[(w * 32 + 4 * kk + r) * 16 + fr] = acc0[r]; part[(w * 32 + 16 + 4 * kk + r) * 16 + fr] = acc1[r]; }
.LBB0_662:
	v_lshl_add_u64 v[194:195], v[84:85], 0, s[0:1]
	global_load_dword v162, v[194:195], off
	global_load_dword v163, v[194:195], off offset:64
	global_load_dword v164, v[194:195], off offset:512
	global_load_dword v165, v[194:195], off offset:576
	global_load_dword v166, v[194:195], off offset:1024
	global_load_dword v167, v[194:195], off offset:1088
	global_load_dword v168, v[194:195], off offset:1536
	global_load_dword v169, v[194:195], off offset:1600
	global_load_dword v170, v[194:195], off offset:2048
	global_load_dword v171, v[194:195], off offset:2112
	global_load_dword v172, v[194:195], off offset:2560
	global_load_dword v173, v[194:195], off offset:2624
	global_load_dword v174, v[194:195], off offset:3072
	global_load_dword v175, v[194:195], off offset:3136
	global_load_dword v176, v[194:195], off offset:3584
	global_load_dword v177, v[194:195], off offset:3648
	ds_read2_b32 v[198:199], v18 offset1:4
	ds_read2_b32 v[200:201], v18 offset0:8 offset1:12
	ds_read2_b32 v[202:203], v18 offset0:16 offset1:20
	ds_read2_b32 v[204:205], v18 offset0:24 offset1:28
	s_add_u32 s0, s0, 0x1000
	s_addc_u32 s1, s1, 0
	v_lshl_add_u64 v[196:197], v[84:85], 0, s[0:1]
	global_load_dword v178, v[196:197], off
	global_load_dword v179, v[196:197], off offset:64
	global_load_dword v180, v[196:197], off offset:512
	global_load_dword v181, v[196:197], off offset:576
	global_load_dword v182, v[196:197], off offset:1024
	global_load_dword v183, v[196:197], off offset:1088
	global_load_dword v184, v[196:197], off offset:1536
	global_load_dword v185, v[196:197], off offset:1600
	global_load_dword v186, v[196:197], off offset:2048
	global_load_dword v187, v[196:197], off offset:2112
	global_load_dword v188, v[196:197], off offset:2560
	global_load_dword v189, v[196:197], off offset:2624
	global_load_dword v190, v[196:197], off offset:3072
	global_load_dword v191, v[196:197], off offset:3136
	global_load_dword v192, v[196:197], off offset:3584
	global_load_dword v193, v[196:197], off offset:3648
	v_add_u32_e32 v18, 0x80, v18
	ds_read2_b32 v[206:207], v18 offset1:4
	ds_read2_b32 v[208:209], v18 offset0:8 offset1:12
	ds_read2_b32 v[210:211], v18 offset0:16 offset1:20
	ds_read2_b32 v[212:213], v18 offset0:24 offset1:28
	s_waitcnt vmcnt(16) lgkmcnt(4)
	v_mfma_f32_16x16x4_f32 v[10:13], v162, v198, v[10:13]
	v_mfma_f32_16x16x4_f32 v[14:17], v163, v198, v[14:17]
	v_mfma_f32_16x16x4_f32 v[10:13], v164, v199, v[10:13]
	v_mfma_f32_16x16x4_f32 v[14:17], v165, v199, v[14:17]
	v_mfma_f32_16x16x4_f32 v[10:13], v166, v200, v[10:13]
	v_mfma_f32_16x16x4_f32 v[14:17], v167, v200, v[14:17]
	v_mfma_f32_16x16x4_f32 v[10:13], v168, v201, v[10:13]
	v_mfma_f32_16x16x4_f32 v[14:17], v169, v201, v[14:17]
	v_mfma_f32_16x16x4_f32 v[10:13], v170, v202, v[10:13]
	v_mfma_f32_16x16x4_f32 v[14:17], v171, v202, v[14:17]
	v_mfma_f32_16x16x4_f32 v[10:13], v172, v203, v[10:13]
	v_mfma_f32_16x16x4_f32 v[14:17], v173, v203, v[14:17]
	v_mfma_f32_16x16x4_f32 v[10:13], v174, v204, v[10:13]
	v_mfma_f32_16x16x4_f32 v[14:17], v175, v204, v[14:17]
	v_mfma_f32_16x16x4_f32 v[10:13], v176, v205, v[10:13]
	v_mfma_f32_16x16x4_f32 v[14:17], v177, v205, v[14:17]
	s_add_u32 s0, s0, 0x1000
	s_addc_u32 s1, s1, 0
	v_lshl_add_u64 v[194:195], v[84:85], 0, s[0:1]
	global_load_dword v162, v[194:195], off
	global_load_dword v163, v[194:195], off offset:64
	global_load_dword v164, v[194:195], off offset:512
	global_load_dword v165, v[194:195], off offset:576
	global_load_dword v166, v[194:195], off offset:1024
	global_load_dword v167, v[194:195], off offset:1088
	global_load_dword v168, v[194:195], off offset:1536
	global_load_dword v169, v[194:195], off offset:1600
	global_load_dword v170, v[194:195], off offset:2048
	global_load_dword v171, v[194:195], off offset:2112
	global_load_dword v172, v[194:195], off offset:2560
	global_load_dword v173, v[194:195], off offset:2624
	global_load_dword v174, v[194:195], off offset:3072
	global_load_dword v175, v[194:195], off offset:3136
	global_load_dword v176, v[194:195], off offset:3584
	global_load_dword v177, v[194:195], off offset:3648
	v_add_u32_e32 v18, 0x80, v18
	ds_read2_b32 v[198:199], v18 offset1:4
	ds_read2_b32 v[200:201], v18 offset0:8 offset1:12
	ds_read2_b32 v[202:203], v18 offset0:16 offset1:20
	ds_read2_b32 v[204:205], v18 offset0:24 offset1:28
	s_waitcnt vmcnt(16) lgkmcnt(4)
	v_mfma_f32_16x16x4_f32 v[10:13], v178, v206, v[10:13]
	v_mfma_f32_16x16x4_f32 v[14:17], v179, v206, v[14:17]
	v_mfma_f32_16x16x4_f32 v[10:13], v180, v207, v[10:13]
	v_mfma_f32_16x16x4_f32 v[14:17], v181, v207, v[14:17]
	v_mfma_f32_16x16x4_f32 v[10:13], v182, v208, v[10:13]
	v_mfma_f32_16x16x4_f32 v[14:17], v183, v208, v[14:17]
	v_mfma_f32_16x16x4_f32 v[10:13], v184, v209, v[10:13]
	v_mfma_f32_16x16x4_f32 v[14:17], v185, v209, v[14:17]
	v_mfma_f32_16x16x4_f32 v[10:13], v186, v210, v[10:13]
	v_mfma_f32_16x16x4_f32 v[14:17], v187, v210, v[14:17]
	v_mfma_f32_16x16x4_f32 v[10:13], v188, v211, v[10:13]
	v_mfma_f32_16x16x4_f32 v[14:17], v189, v211, v[14:17]
	v_mfma_f32_16x16x4_f32 v[10:13], v190, v212, v[10:13]
	v_mfma_f32_16x16x4_f32 v[14:17], v191, v212, v[14:17]
	v_mfma_f32_16x16x4_f32 v[10:13], v192, v213, v[10:13]
	v_mfma_f32_16x16x4_f32 v[14:17], v193, v213, v[14:17]
	s_add_u32 s0, s0, 0x1000
	s_addc_u32 s1, s1, 0
	v_lshl_add_u64 v[196:197], v[84:85], 0, s[0:1]
	global_load_dword v178, v[196:197], off
	global_load_dword v179, v[196:197], off offset:64
	global_load_dword v180, v[196:197], off offset:512
	global_load_dword v181, v[196:197], off offset:576
	global_load_dword v182, v[196:197], off offset:1024
	global_load_dword v183, v[196:197], off offset:1088
	global_load_dword v184, v[196:197], off offset:1536
	global_load_dword v185, v[196:197], off offset:1600
	global_load_dword v186, v[196:197], off offset:2048
	global_load_dword v187, v[196:197], off offset:2112
	global_load_dword v188, v[196:197], off offset:2560
	global_load_dword v189, v[196:197], off offset:2624
	global_load_dword v190, v[196:197], off offset:3072
	global_load_dword v191, v[196:197], off offset:3136
	global_load_dword v192, v[196:197], off offset:3584
	global_load_dword v193, v[196:197], off offset:3648
	v_add_u32_e32 v18, 0x80, v18
	ds_read2_b32 v[206:207], v18 offset1:4
	ds_read2_b32 v[208:209], v18 offset0:8 offset1:12
	ds_read2_b32 v[210:211], v18 offset0:16 offset1:20
	ds_read2_b32 v[212:213], v18 offset0:24 offset1:28
	s_waitcnt vmcnt(16) lgkmcnt(4)
; __device__ __forceinline__ void phase_router(const Args& a, LAS unsigned char* lds) {
;     ...
;                 for (int ks = 0; ks < 64; ++ks) { const float b = hp[ks * 4], a0 = wp[(size_t)ks * 128], a1 = wp[(size_t)ks * 128 + 16];
;                     acc0 = __builtin_amdgcn_mfma_f32_16x16x4f32(a0, b, acc0, 0, 0, 0); acc1 = __builtin_amdgcn_mfma_f32_16x16x4f32(a1, b, acc1, 0, 0, 0); }
	v_mfma_f32_16x16x4_f32 v[10:13], v162, v198, v[10:13]
	v_mfma_f32_16x16x4_f32 v[14:17], v163, v198, v[14:17]
	v_mfma_f32_16x16x4_f32 v[10:13], v164, v199, v[10:13]
	v_mfma_f32_16x16x4_f32 v[14:17], v165, v199, v[14:17]
	v_mfma_f32_16x16x4_f32 v[10:13], v166, v200, v[10:13]
	v_mfma_f32_16x16x4_f32 v[14:17], v167, v200, v[14:17]
	v_mfma_f32_16x16x4_f32 v[10:13], v168, v201, v[10:13]
	v_mfma_f32_16x16x4_f32 v[14:17], v169, v201, v[14:17]
	v_mfma_f32_16x16x4_f32 v[10:13], v170, v202, v[10:13]
	v_mfma_f32_16x16x4_f32 v[14:17], v171, v202, v[14:17]
	v_mfma_f32_16x16x4_f32 v[10:13], v172, v203, v[10:13]
	v_mfma_f32_16x16x4_f32 v[14:17], v173, v203, v[14:17]
	v_mfma_f32_16x16x4_f32 v[10:13], v174, v204, v[10:13]
	v_mfma_f32_16x16x4_f32 v[14:17], v175, v204, v[14:17]
	v_mfma_f32_16x16x4_f32 v[10:13], v176, v205, v[10:13]
	v_mfma_f32_16x16x4_f32 v[14:17], v177, v205, v[14:17]
	s_add_u32 s0, s0, 0x1000
	s_addc_u32 s1, s1, 0
	v_lshl_add_u64 v[194:195], v[84:85], 0, s[0:1]
	global_load_dword v162, v[194:195], off
	global_load_dword v163, v[194:195], off offset:64
	global_load_dword v164, v[194:195], off offset:512
	global_load_dword v165, v[194:195], off offset:576
	global_load_dword v166, v[194:195], off offset:1024
	global_load_dword v167, v[194:195], off offset:1088
	global_load_dword v168, v[194:195], off offset:1536
	global_load_dword v169, v[194:195], off offset:1600
	global_load_dword v170, v[194:195], off offset:2048
	global_load_dword v171, v[194:195], off offset:2112
	global_load_dword v172, v[194:195], off offset:2560
	global_load_dword v173, v[194:195], off offset:2624
	global_load_dword v174, v[194:195], off offset:3072
	global_load_dword v175, v[194:195], off offset:3136
	global_load_dword v176, v[194:195], off offset:3584
	global_load_dword v177, v[194:195], off offset:3648
	v_add_u32_e32 v18, 0x80, v18
	ds_read2_b32 v[198:199], v18 offset1:4
	ds_read2_b32 v[200:201], v18 offset0:8 offset1:12
	ds_read2_b32 v[202:203], v18 offset0:16 offset1:20
	ds_read2_b32 v[204:205], v18 offset0:24 offset1:28
	s_waitcnt vmcnt(16) lgkmcnt(4)
	v_mfma_f32_16x16x4_f32 v[10:13], v178, v206, v[10:13]
	v_mfma_f32_16x16x4_f32 v[14:17], v179, v206, v[14:17]
	v_mfma_f32_16x16x4_f32 v[10:13], v180, v207, v[10:13]
	v_mfma_f32_16x16x4_f32 v[14:17], v181, v207, v[14:17]
	v_mfma_f32_16x16x4_f32 v[10:13], v182, v208, v[10:13]
	v_mfma_f32_16x16x4_f32 v[14:17], v183, v208, v[14:17]
	v_mfma_f32_16x16x4_f32 v[10:13], v184, v209, v[10:13]
	v_mfma_f32_16x16x4_f32 v[14:17], v185, v209, v[14:17]
	v_mfma_f32_16x16x4_f32 v[10:13], v186, v210, v[10:13]
	v_mfma_f32_16x16x4_f32 v[14:17], v187, v210, v[14:17]
	v_mfma_f32_16x16x4_f32 v[10:13], v188, v211, v[10:13]
	v_mfma_f32_16x16x4_f32 v[14:17], v189, v211, v[14:17]
	v_mfma_f32_16x16x4_f32 v[10:13], v190, v212, v[10:13]
	v_mfma_f32_16x16x4_f32 v[14:17], v191, v212, v[14:17]
	v_mfma_f32_16x16x4_f32 v[10:13], v192, v213, v[10:13]
	v_mfma_f32_16x16x4_f32 v[14:17], v193, v213, v[14:17]
	s_add_u32 s0, s0, 0x1000
	s_addc_u32 s1, s1, 0
	v_lshl_add_u64 v[196:197], v[84:85], 0, s[0:1]
	global_load_dword v178, v[196:197], off
	global_load_dword v179, v[196:197], off offset:64
	global_load_dword v180, v[196:197], off offset:512
	global_load_dword v181, v[196:197], off offset:576
	global_load_dword v182, v[196:197], off offset:1024
	global_load_dword v183, v[196:197], off offset:1088
	global_load_dword v184, v[196:197], off offset:1536
	global_load_dword v185, v[196:197], off offset:1600
	global_load_dword v186, v[196:197], off offset:2048
	global_load_dword v187, v[196:197], off offset:2112
	global_load_dword v188, v[196:197], off offset:2560
	global_load_dword v189, v[196:197], off offset:2624
	global_load_dword v190, v[196:197], off offset:3072
	global_load_dword v191, v[196:197], off offset:3136
	global_load_dword v192, v[196:197], off offset:3584
	global_load_dword v193, v[196:197], off offset:3648
	v_add_u32_e32 v18, 0x80, v18
	ds_read2_b32 v[206:207], v18 offset1:4
	ds_read2_b32 v[208:209], v18 offset0:8 offset1:12
	ds_read2_b32 v[210:211], v18 offset0:16 offset1:20
	ds_read2_b32 v[212:213], v18 offset0:24 offset1:28
	s_waitcnt vmcnt(16) lgkmcnt(4)
	v_mfma_f32_16x16x4_f32 v[10:13], v162, v198, v[10:13]
	v_mfma_f32_16x16x4_f32 v[14:17], v163, v198, v[14:17]
	v_mfma_f32_16x16x4_f32 v[10:13], v164, v199, v[10:13]
	v_mfma_f32_16x16x4_f32 v[14:17], v165, v199, v[14:17]
	v_mfma_f32_16x16x4_f32 v[10:13], v166, v200, v[10:13]
	v_mfma_f32_16x16x4_f32 v[14:17], v167, v200, v[14:17]
	v_mfma_f32_16x16x4_f32 v[10:13], v168, v201, v[10:13]
	v_mfma_f32_16x16x4_f32 v[14:17], v169, v201, v[14:17]
	v_mfma_f32_16x16x4_f32 v[10:13], v170, v202, v[10:13]
	v_mfma_f32_16x16x4_f32 v[14:17], v171, v202, v[14:17]
	v_mfma_f32_16x16x4_f32 v[10:13], v172, v203, v[10:13]
	v_mfma_f32_16x16x4_f32 v[14:17], v173, v203, v[14:17]
	v_mfma_f32_16x16x4_f32 v[10:13], v174, v204, v[10:13]
	v_mfma_f32_16x16x4_f32 v[14:17], v175, v204, v[14:17]
	v_mfma_f32_16x16x4_f32 v[10:13], v176, v205, v[10:13]
	v_mfma_f32_16x16x4_f32 v[14:17], v177, v205, v[14:17]
	s_add_u32 s0, s0, 0x1000
	s_addc_u32 s1, s1, 0
	v_lshl_add_u64 v[194:195], v[84:85], 0, s[0:1]
	global_load_dword v162, v[194:195], off
	global_load_dword v163, v[194:195], off offset:64
	global_load_dword v164, v[194:195], off offset:512
	global_load_dword v165, v[194:195], off offset:576
	global_load_dword v166, v[194:195], off offset:1024
	global_load_dword v167, v[194:195], off offset:1088
	global_load_dword v168, v[194:195], off offset:1536
	global_load_dword v169, v[194:195], off offset:1600
	global_load_dword v170, v[194:195], off offset:2048
	global_load_dword v171, v[194:195], off offset:2112
	global_load_dword v172, v[194:195], off offset:2560
	global_load_dword v173, v[194:195], off offset:2624
	global_load_dword v174, v[194:195], off offset:3072
	global_load_dword v175, v[194:195], off offset:3136
	global_load_dword v176, v[194:195], off offset:3584
	global_load_dword v177, v[194:195], off offset:3648
	v_add_u32_e32 v18, 0x80, v18
	ds_read2_b32 v[198:199], v18 offset1:4
	ds_read2_b32 v[200:201], v18 offset0:8 offset1:12
	ds_read2_b32 v[202:203], v18 offset0:16 offset1:20
	ds_read2_b32 v[204:205], v18 offset0:24 offset1:28
	s_waitcnt vmcnt(16) lgkmcnt(4)
; __device__ __forceinline__ void phase_router(const Args& a, LAS unsigned char* lds) {
;     ...
;                 for (int ks = 0; ks < 64; ++ks) { const float b = hp[ks * 4], a0 = wp[(size_t)ks * 128], a1 = wp[(size_t)ks * 128 + 16];
;                     acc0 = __builtin_amdgcn_mfma_f32_16x16x4f32(a0, b, acc0, 0, 0, 0); acc1 = __builtin_amdgcn_mfma_f32_16x16x4f32(a1, b, acc1, 0, 0, 0); }
; #pragma unroll
;                 for (int r = 0; r < 4; ++r) { part[(w * 32 + 4 * kk + r) * 16 + fr] = acc0[r]; part[(w * 32 + 16 + 4 * kk + r) * 16 + fr] = acc1[r]; }
;             }
;             __syncthreads();
;             {
;                 const int tl = tid >> 5, e = tid & 31; float s = brt;
; #pragma unroll
;                 for (int q = 0; q < 8; ++q) s += part[(q * 32 + e) * 16 + tl];
;                 bool taken = false; float tv[4]; int te[4];
; #pragma unroll
;                 for (int r = 0; r < 4; ++r) { float bv = taken ? -INFINITY : s; int be = e;
; #pragma unroll
;                     for (int off = 16; off >= 1; off >>= 1) { const float ov = __shfl_xor(bv, off); const int oe = __shfl_xor(be, off); if (ov > bv || (ov == bv && oe < be)) { bv = ov; be = oe; } }
;                     tv[r] = bv; te[r] = be; if (be == e) taken = true; }
	v_mfma_f32_16x16x4_f32 v[10:13], v178, v206, v[10:13]
	v_mfma_f32_16x16x4_f32 v[14:17], v179, v206, v[14:17]
	v_mfma_f32_16x16x4_f32 v[10:13], v180, v207, v[10:13]
	v_mfma_f32_16x16x4_f32 v[14:17], v181, v207, v[14:17]
	v_mfma_f32_16x16x4_f32 v[10:13], v182, v208, v[10:13]
	v_mfma_f32_16x16x4_f32 v[14:17], v183, v208, v[14:17]
	v_mfma_f32_16x16x4_f32 v[10:13], v184, v209, v[10:13]
	v_mfma_f32_16x16x4_f32 v[14:17], v185, v209, v[14:17]
	v_mfma_f32_16x16x4_f32 v[10:13], v186, v210, v[10:13]
	v_mfma_f32_16x16x4_f32 v[14:17], v187, v210, v[14:17]
	v_mfma_f32_16x16x4_f32 v[10:13], v188, v211, v[10:13]
	v_mfma_f32_16x16x4_f32 v[14:17], v189, v211, v[14:17]
	v_mfma_f32_16x16x4_f32 v[10:13], v190, v212, v[10:13]
	v_mfma_f32_16x16x4_f32 v[14:17], v191, v212, v[14:17]
	v_mfma_f32_16x16x4_f32 v[10:13], v192, v213, v[10:13]
	v_mfma_f32_16x16x4_f32 v[14:17], v193, v213, v[14:17]
	s_add_u32 s0, s0, 0x1000
	s_addc_u32 s1, s1, 0
	v_lshl_add_u64 v[196:197], v[84:85], 0, s[0:1]
	global_load_dword v178, v[196:197], off
	global_load_dword v179, v[196:197], off offset:64
	global_load_dword v180, v[196:197], off offset:512
	global_load_dword v181, v[196:197], off offset:576
	global_load_dword v182, v[196:197], off offset:1024
	global_load_dword v183, v[196:197], off offset:1088
	global_load_dword v184, v[196:197], off offset:1536
	global_load_dword v185, v[196:197], off offset:1600
	global_load_dword v186, v[196:197], off offset:2048
	global_load_dword v187, v[196:197], off offset:2112
	global_load_dword v188, v[196:197], off offset:2560
	global_load_dword v189, v[196:197], off offset:2624
	global_load_dword v190, v[196:197], off offset:3072
	global_load_dword v191, v[196:197], off offset:3136
	global_load_dword v192, v[196:197], off offset:3584
	global_load_dword v193, v[196:197], off offset:3648
	v_add_u32_e32 v18, 0x80, v18
	ds_read2_b32 v[206:207], v18 offset1:4
	ds_read2_b32 v[208:209], v18 offset0:8 offset1:12
	ds_read2_b32 v[210:211], v18 offset0:16 offset1:20
	ds_read2_b32 v[212:213], v18 offset0:24 offset1:28
	s_waitcnt vmcnt(16) lgkmcnt(4)
	v_mfma_f32_16x16x4_f32 v[10:13], v162, v198, v[10:13]
	v_mfma_f32_16x16x4_f32 v[14:17], v163, v198, v[14:17]
	v_mfma_f32_16x16x4_f32 v[10:13], v164, v199, v[10:13]
	v_mfma_f32_16x16x4_f32 v[14:17], v165, v199, v[14:17]
	v_mfma_f32_16x16x4_f32 v[10:13], v166, v200, v[10:13]
	v_mfma_f32_16x16x4_f32 v[14:17], v167, v200, v[14:17]
	v_mfma_f32_16x16x4_f32 v[10:13], v168, v201, v[10:13]
	v_mfma_f32_16x16x4_f32 v[14:17], v169, v201, v[14:17]
	v_mfma_f32_16x16x4_f32 v[10:13], v170, v202, v[10:13]
	v_mfma_f32_16x16x4_f32 v[14:17], v171, v202, v[14:17]
	v_mfma_f32_16x16x4_f32 v[10:13], v172, v203, v[10:13]
	v_mfma_f32_16x16x4_f32 v[14:17], v173, v203, v[14:17]
	v_mfma_f32_16x16x4_f32 v[10:13], v174, v204, v[10:13]
	v_mfma_f32_16x16x4_f32 v[14:17], v175, v204, v[14:17]
	v_mfma_f32_16x16x4_f32 v[10:13], v176, v205, v[10:13]
	v_mfma_f32_16x16x4_f32 v[14:17], v177, v205, v[14:17]
	s_waitcnt vmcnt(0) lgkmcnt(0)
	v_mfma_f32_16x16x4_f32 v[10:13], v178, v206, v[10:13]
	v_mfma_f32_16x16x4_f32 v[14:17], v179, v206, v[14:17]
	v_mfma_f32_16x16x4_f32 v[10:13], v180, v207, v[10:13]
	v_mfma_f32_16x16x4_f32 v[14:17], v181, v207, v[14:17]
	v_mfma_f32_16x16x4_f32 v[10:13], v182, v208, v[10:13]
	v_mfma_f32_16x16x4_f32 v[14:17], v183, v208, v[14:17]
	v_mfma_f32_16x16x4_f32 v[10:13], v184, v209, v[10:13]
	v_mfma_f32_16x16x4_f32 v[14:17], v185, v209, v[14:17]
	v_mfma_f32_16x16x4_f32 v[10:13], v186, v210, v[10:13]
	v_mfma_f32_16x16x4_f32 v[14:17], v187, v210, v[14:17]
	v_mfma_f32_16x16x4_f32 v[10:13], v188, v211, v[10:13]
	v_mfma_f32_16x16x4_f32 v[14:17], v189, v211, v[14:17]
	v_mfma_f32_16x16x4_f32 v[10:13], v190, v212, v[10:13]
	v_mfma_f32_16x16x4_f32 v[14:17], v191, v212, v[14:17]
	v_mfma_f32_16x16x4_f32 v[10:13], v192, v213, v[10:13]
	v_mfma_f32_16x16x4_f32 v[14:17], v193, v213, v[14:17]
	s_add_u32 s0, s0, 0x1000
	s_addc_u32 s1, s1, 0
	v_add_u32_e32 v18, 0x80, v18
	s_nop 2
	v_add_u32_e32 v2, v120, v129
	s_nop 4
	ds_write2st64_b32 v128, v10, v14 offset1:4
	ds_write_b32 v2, v11
	ds_write_b32 v130, v15
	v_add_u32_e32 v2, v120, v131
	ds_write_b32 v2, v12
	ds_write_b32 v132, v16
	v_add_u32_e32 v2, v120, v133
	ds_write_b32 v2, v13
	ds_write_b32 v134, v17
	s_waitcnt lgkmcnt(0)
	s_barrier
	ds_read2st64_b32 v[2:3], v122 offset1:8
	ds_read2st64_b32 v[4:5], v122 offset0:16 offset1:24
	ds_read2st64_b32 v[6:7], v122 offset0:32 offset1:40
	s_waitcnt lgkmcnt(2)
	v_add_f32_e32 v2, v105, v2
	v_add_f32_e32 v8, v2, v3
	ds_read2st64_b32 v[2:3], v122 offset0:48 offset1:56
	s_waitcnt lgkmcnt(2)
	v_add_f32_e32 v4, v8, v4
	v_add_f32_e32 v4, v4, v5
	s_waitcnt lgkmcnt(1)
	v_add_f32_e32 v4, v4, v6
	v_add_f32_e32 v4, v4, v7
	s_waitcnt lgkmcnt(0)
	v_add_f32_e32 v2, v4, v2
	v_add_f32_e32 v5, v2, v3
	ds_bpermute_b32 v4, v117, v5
	ds_bpermute_b32 v7, v117, v1
	s_waitcnt lgkmcnt(1)
	v_cmp_lt_f32_e64 s[10:11], v5, v4
	v_cmp_nlt_f32_e32 vcc, v5, v4
	s_and_saveexec_b64 s[36:37], vcc
	s_cbranch_execz .LBB0_665
	v_cmp_eq_f32_e32 vcc, v5, v4
	s_waitcnt lgkmcnt(0)
	v_cmp_lt_i32_e64 s[0:1], v7, v1
	s_and_b64 s[0:1], vcc, s[0:1]
	s_andn2_b64 s[10:11], s[10:11], exec
	s_and_b64 s[0:1], s[0:1], exec
	s_or_b64 s[10:11], s[10:11], s[0:1]
